# P8: first K-loop trip peeled with srcC=0 in the first-K-tile MFMA intervals; the 32 accumulator-clearing MFMAs per wave and unit removed
# speedup vs baseline: 1.0071x; 1.0024x over previous
; #define PG8_STAGE(bufoff, gbase, voff) do { PG8_GLDS((const char*)(gbase), (voff)[0], ldsb + (bufoff)); PG8_GLDS((const char*)(gbase), (voff)[1], ldsb + (bufoff) + 8192u); } while (0)
; #define PG8_STAGEA(bufoff, gbase, o0, o1) do { PG8_GLDS((const char*)(gbase), (o0), ldsb + (bufoff)); PG8_GLDS((const char*)(gbase), (o1), ldsb + (bufoff) + 8192u); } while (0)
; #define PG8_STAGEA1(bufoff, gbase) do { if constexpr (Sched::GATHER) { PG8_STAGEA(bufoff, gbase, vA2, vA3); } else { PG8_STAGEA(bufoff, (gbase) + hstep, vA0, vA1); } } while (0)
; #define PG8_WAIT_V(n) asm volatile("s_waitcnt vmcnt(" #n ")" ::: "memory")
; #define PG8_BAR __builtin_amdgcn_s_barrier()
; template <class Epi, class Sched, bool F8 = false, bool PF = false, bool I8 = false, int PID = -1>
; __device__ __forceinline__ void gemm_phase(LAS unsigned char* lds, LAS unsigned char* xlds, const int RP, const int RPB, const int nt, const Sched& S, const Epi& E, const int stagger_ticks) {
;     ...
;     if (Sched::GATHER) { unsigned v[4] = {vA0, vA1, vA2, vA3}; if (has_next) S.a_offsets(nxt, Rr, Cc, RP, v); *nslot = (u32x4){v[0], v[1], v[2], v[3]}; }
;     PG8_ZERO_ACC();
;     PG8_STAGE(PG8_SB(0, 0), cB, voffB); PG8_STAGE(PG8_SB(0, 1), cB + hstepB, voffB); PG8_STAGEA(PG8_SA(0, 0), cA, vA0, vA1); PG8_STAGEA1(PG8_SA(0, 1), cA);
;     if (wr == 1) PG8_BAR;
;     PG8_WAIT_V(2); PG8_BAR;
;     PG8_STAGE(PG8_SB(1, 0), cB + kstep, voffB); PG8_STAGEA(PG8_SA(1, 0), cA + kstep, vA0, vA1); PG8_STAGE(PG8_SB(1, 1), cB + hstepB + kstep, voffB);
;     PG8_WAIT_V(6); PG8_BAR;
.LBB0_952:
	v_lshl_add_u32 v9, v6, 4, 0
	v_add_u32_e32 v203, 0x20800, v9
	v_lshlrev_b32_e32 v9, 1, v1
	v_lshlrev_b32_e32 v10, 2, v1
	v_lshrrev_b32_e32 v11, 2, v1
	v_and_b32_e32 v7, 3, v7
	v_and_b32_e32 v9, 0x3fffc0, v9
	v_and_b32_e32 v11, 4, v11
	v_and_or_b32 v7, v10, 48, v7
	s_ashr_i32 s3, s14, 6
	v_mov_b32_e32 v198, 0
	v_or3_b32 v7, v7, v9, v11
	s_lshl_b32 s12, s3, 10
	v_mov_b32_e32 v199, v198
	v_lshl_add_u32 v204, v7, 10, v201
	v_lshlrev_b32_e32 v7, 1, v200
	v_lshlrev_b32_e32 v9, 2, v200
	v_lshrrev_b32_e32 v10, 2, v200
	v_and_b32_e32 v8, 3, v8
	s_add_i32 s42, s12, 0
	ds_write_b128 v203, v[2:5]
	v_mov_b64_e32 v[2:3], v[198:199]
	v_and_b32_e32 v7, 0x3fffc0, v7
	v_and_b32_e32 v10, 4, v10
	v_and_or_b32 v8, v9, 48, v8
	s_add_i32 s12, s42, 0x10000
	s_ashr_i32 s2, s14, 8
	v_or3_b32 v7, v8, v7, v10
	s_mov_b32 m0, s12
	s_nop 0
	global_load_lds_dwordx4 v204, s[8:9]
	s_add_i32 s12, s42, 0x12000
	v_lshl_add_u32 v205, v7, 10, v202
	s_mov_b32 m0, s12
	s_nop 0
	global_load_lds_dwordx4 v205, s[8:9]
	s_add_u32 s12, s8, 0x2000
	s_addc_u32 s13, s9, 0
	s_add_i32 s15, s42, 0x14000
	s_mov_b32 m0, s15
	s_nop 0
	global_load_lds_dwordx4 v204, s[12:13]
	s_add_i32 s15, s42, 0x16000
	s_mov_b32 m0, s15
	s_nop 0
	global_load_lds_dwordx4 v205, s[12:13]
	s_add_i32 s12, s42, 0x2000
	s_mov_b32 m0, s42
	s_nop 0
	global_load_lds_dwordx4 v66, s[6:7]
	s_add_i32 s15, s42, 0x6000
	s_mov_b32 m0, s12
	s_nop 0
	global_load_lds_dwordx4 v67, s[6:7]
	s_add_i32 s12, s42, 0x4000
	s_mov_b32 m0, s12
	s_nop 0
	global_load_lds_dwordx4 v68, s[6:7]
	s_cmp_eq_u32 s2, 1
	s_mov_b32 m0, s15
	s_nop 0
	global_load_lds_dwordx4 v69, s[6:7]
	s_mov_b32 s43, 0
	s_cselect_b64 s[12:13], -1, 0
	s_cmp_lg_u32 s2, 1
	s_cbranch_scc1 .LBB0_954
	s_barrier

; #define PG8_STAGE(bufoff, gbase, voff) do { PG8_GLDS((const char*)(gbase), (voff)[0], ldsb + (bufoff)); PG8_GLDS((const char*)(gbase), (voff)[1], ldsb + (bufoff) + 8192u); } while (0)
; #define PG8_STAGEA(bufoff, gbase, o0, o1) do { PG8_GLDS((const char*)(gbase), (o0), ldsb + (bufoff)); PG8_GLDS((const char*)(gbase), (o1), ldsb + (bufoff) + 8192u); } while (0)
; #define PG8_STAGEA1(bufoff, gbase) do { if constexpr (Sched::GATHER) { PG8_STAGEA(bufoff, gbase, vA2, vA3); } else { PG8_STAGEA(bufoff, (gbase) + hstep, vA0, vA1); } } while (0)
; template <class Epi, class Sched, bool F8 = false, bool PF = false, bool I8 = false, int PID = -1>
; __device__ __forceinline__ void gemm_phase(LAS unsigned char* lds, LAS unsigned char* xlds, const int RP, const int RPB, const int nt, const Sched& S, const Epi& E, const int stagger_ticks) {
;     ...
;         for (int t = 0; t < nt; t += 2) {
;             const bool last = (t == nt - 2);
;             unsigned ldsb = ldsb0; asm volatile("" : "+s"(ldsb));
;             const char* a1 = cA + (size_t)(t + 1) * kstep;
;             const char* a2 = last ? nA : cA + (size_t)(t + 2) * kstep; const char* b2 = last ? nB : cB + (size_t)(t + 2) * kstep;
;             const char* a3 = a2 + kstep; const char* b3 = b2 + kstep;
;             if constexpr (PF) { const char* pfa = (t + 4 < nt) ? cA + (size_t)(t + 4) * kstep : nA + (size_t)(t + 4 - nt) * kstep;
;                 asm volatile("s_mov_b32 m0, %2\n\ts_nop 0\n\tglobal_load_lds_dword %0, %1" :: "v"(voffP), "s"(pfa), "s"(ldsP) : "memory", "m0"); }
;             const bool relax = (Epi::RELAX > 0) && (t == 0) && epi_ran;
;             PG8_LDB(B0, 0, 0); PG8_LDB(B1, 0, 1); PG8_SCHED; PG8_LDA(At, 0, 0); PG8_STAGEA1(PG8_SA(1, 1), a1);
;             if (Sched::GATHER) { if (last) { const u32x4 nv = *nslot; vA0 = nv.x; vA1 = nv.y; vA2 = nv.z; vA3 = nv.w; } }
;             PG8_WAIT_VX(); PG8_WAIT_L(0); PG8_BAR; PG8_MMA(0, 0, At, B0); PG8_MMA(0, 1, At, B1); PG8_BAR; PG8_SCHED;
;             if constexpr (Epi::BIAS_DMA) { if (t == 0 && has_next) E.bias_dma(nxt, xlds + 8192 + ((ui + 1) & 1) * Epi::BIAS_STRIDE, wid, lane); }
;             PG8_LDA(At, 0, 1); PG8_STAGE(PG8_SB(0, 0), b2, voffB); PG8_STAGE(PG8_SB(0, 1), b2 + hstepB, voffB); PG8_STAGEA(PG8_SA(0, 0), a2, vA0, vA1);
;             PG8_WAIT_VX(); PG8_WAIT_L(0); PG8_BAR; PG8_MMA(1, 0, At, B0); PG8_MMA(1, 1, At, B1); PG8_BAR; PG8_SCHED;
.LBB0_959:
	s_mov_b32 s65, s42
	v_add_u32_e32 v2, 0x10000, v206
	v_add_u32_e32 v14, 0x14000, v206
	ds_read_b128 v[18:21], v2
	ds_read_b128 v[22:25], v2 offset:1024
	ds_read_b128 v[26:29], v2 offset:2048
	ds_read_b128 v[30:33], v2 offset:3072
	ds_read_b128 v[2:5], v14
	ds_read_b128 v[6:9], v14 offset:1024
	ds_read_b128 v[10:13], v14 offset:2048
	ds_read_b128 v[14:17], v14 offset:3072
	s_cmp_eq_u32 s64, 4
	s_cselect_b64 s[26:27], -1, 0
	s_add_i32 s24, s65, 0xc000
	s_add_i32 s25, s65, 0xe000
	s_cmp_lg_u32 s64, 4
	ds_read_b128 v[58:61], v207
	ds_read_b128 v[62:65], v207 offset:1024
	ds_read_b128 v[50:53], v207 offset:2048
	ds_read_b128 v[54:57], v207 offset:3072
	ds_read_b128 v[42:45], v207 offset:4096
	ds_read_b128 v[46:49], v207 offset:5120
	ds_read_b128 v[34:37], v207 offset:6144
	ds_read_b128 v[38:41], v207 offset:7168
	s_mov_b32 m0, s24
	s_nop 0
	global_load_lds_dwordx4 v68, s[2:3]
	s_nop 0
	s_mov_b32 m0, s25
	s_nop 0
	global_load_lds_dwordx4 v69, s[2:3]
	s_cbranch_scc1 .LBB0_958
	ds_read_b128 v[66:69], v203
	s_branch .LBB0_958
.Lmy_z959:
	s_mov_b32 s65, s42
	v_add_u32_e32 v2, 0x10000, v206
	v_add_u32_e32 v14, 0x14000, v206
	ds_read_b128 v[18:21], v2
	ds_read_b128 v[22:25], v2 offset:1024
	ds_read_b128 v[26:29], v2 offset:2048
	ds_read_b128 v[30:33], v2 offset:3072
	ds_read_b128 v[2:5], v14
	ds_read_b128 v[6:9], v14 offset:1024
	ds_read_b128 v[10:13], v14 offset:2048
	ds_read_b128 v[14:17], v14 offset:3072
	s_cmp_eq_u32 s64, 4
	s_cselect_b64 s[26:27], -1, 0
	s_add_i32 s24, s65, 0xc000
	s_add_i32 s25, s65, 0xe000
	s_cmp_lg_u32 s64, 4
	ds_read_b128 v[58:61], v207
	ds_read_b128 v[62:65], v207 offset:1024
	ds_read_b128 v[50:53], v207 offset:2048
	ds_read_b128 v[54:57], v207 offset:3072
	ds_read_b128 v[42:45], v207 offset:4096
	ds_read_b128 v[46:49], v207 offset:5120
	ds_read_b128 v[34:37], v207 offset:6144
	ds_read_b128 v[38:41], v207 offset:7168
	s_mov_b32 m0, s24
	s_nop 0
	global_load_lds_dwordx4 v68, s[2:3]
	s_nop 0
	s_mov_b32 m0, s25
	s_nop 0
	global_load_lds_dwordx4 v69, s[2:3]
	s_cbranch_scc1 .Lmy_z958
	ds_read_b128 v[66:69], v203
	s_branch .Lmy_z958
.Lmy_z958:
	s_add_u32 s28, s2, 0x80
	s_addc_u32 s29, s3, 0
	s_and_b64 s[24:25], s[26:27], exec
	s_cselect_b32 s28, s20, s28
	s_cselect_b32 s29, s21, s29
	s_add_u32 s24, s28, 0x80
	s_addc_u32 s25, s29, 0
	s_waitcnt vmcnt(8)
	s_and_b64 s[26:27], s[26:27], exec
	s_waitcnt lgkmcnt(0)
	s_cselect_b32 s26, s8, s23
	s_cselect_b32 s27, s9, s63
	s_add_u32 s30, s26, 0x80
	s_addc_u32 s31, s27, 0
	s_barrier
	s_setprio 1
	s_waitcnt lgkmcnt(6)
	v_mfma_f32_16x16x128_f8f6f4 v[186:189], v[18:25], v[58:65], 0
	v_mfma_f32_16x16x128_f8f6f4 v[194:197], v[26:33], v[58:65], 0
	s_waitcnt lgkmcnt(4)
	v_mfma_f32_16x16x128_f8f6f4 v[190:193], v[18:25], v[50:57], 0
	v_mfma_f32_16x16x128_f8f6f4 v[182:185], v[26:33], v[50:57], 0
	s_waitcnt lgkmcnt(2)
	v_mfma_f32_16x16x128_f8f6f4 v[154:157], v[18:25], v[42:49], 0
	v_mfma_f32_16x16x128_f8f6f4 v[150:153], v[26:33], v[42:49], 0
	s_waitcnt lgkmcnt(0)
	v_mfma_f32_16x16x128_f8f6f4 v[138:141], v[18:25], v[34:41], 0
	v_mfma_f32_16x16x128_f8f6f4 v[134:137], v[26:33], v[34:41], 0
	s_setprio 0
	s_setprio 1
	v_mfma_f32_16x16x128_f8f6f4 v[174:177], v[2:9], v[58:65], 0
	v_mfma_f32_16x16x128_f8f6f4 v[178:181], v[10:17], v[58:65], 0
	v_mfma_f32_16x16x128_f8f6f4 v[170:173], v[2:9], v[50:57], 0
	v_mfma_f32_16x16x128_f8f6f4 v[166:169], v[10:17], v[50:57], 0
	v_mfma_f32_16x16x128_f8f6f4 v[162:165], v[2:9], v[42:49], 0
	v_mfma_f32_16x16x128_f8f6f4 v[158:161], v[10:17], v[42:49], 0
	v_mfma_f32_16x16x128_f8f6f4 v[146:149], v[2:9], v[34:41], 0
	v_mfma_f32_16x16x128_f8f6f4 v[142:145], v[10:17], v[34:41], 0
	s_setprio 0
	s_barrier
	ds_read_b128 v[34:37], v207 offset:16384
	ds_read_b128 v[38:41], v207 offset:17408
	ds_read_b128 v[42:45], v207 offset:18432
	ds_read_b128 v[46:49], v207 offset:19456
	ds_read_b128 v[50:53], v207 offset:20480
	ds_read_b128 v[54:57], v207 offset:21504
	ds_read_b128 v[58:61], v207 offset:22528
	ds_read_b128 v[62:65], v207 offset:23552
	s_add_i32 s66, s65, 0x10000
	s_mov_b32 m0, s66
	s_nop 0
	global_load_lds_dwordx4 v204, s[26:27]
	s_add_i32 s66, s65, 0x12000
	s_mov_b32 m0, s66
	s_nop 0
	global_load_lds_dwordx4 v205, s[26:27]
	s_add_u32 s66, s26, 0x2000
	s_addc_u32 s67, s27, 0
	s_add_i32 s68, s65, 0x14000
	s_mov_b32 m0, s68
	s_nop 0
	global_load_lds_dwordx4 v204, s[66:67]
	s_add_i32 s68, s65, 0x16000
	s_mov_b32 m0, s68
	s_nop 0
	global_load_lds_dwordx4 v205, s[66:67]
	s_waitcnt vmcnt(6)
	s_waitcnt lgkmcnt(0)
	s_barrier
	s_setprio 1
	s_waitcnt lgkmcnt(6)
	v_mfma_f32_16x16x128_f8f6f4 v[122:125], v[18:25], v[34:41], 0
	v_mfma_f32_16x16x128_f8f6f4 v[118:121], v[26:33], v[34:41], 0
	s_waitcnt lgkmcnt(4)
	v_mfma_f32_16x16x128_f8f6f4 v[106:109], v[18:25], v[42:49], 0
	v_mfma_f32_16x16x128_f8f6f4 v[102:105], v[26:33], v[42:49], 0
	s_mov_b32 m0, s65
	s_nop 0
	global_load_lds_dwordx4 v66, s[28:29]
	s_waitcnt lgkmcnt(2)
	v_mfma_f32_16x16x128_f8f6f4 v[90:93], v[18:25], v[50:57], 0
	v_mfma_f32_16x16x128_f8f6f4 v[86:89], v[26:33], v[50:57], 0
	s_waitcnt lgkmcnt(0)
	v_mfma_f32_16x16x128_f8f6f4 v[74:77], v[18:25], v[58:65], 0
	v_mfma_f32_16x16x128_f8f6f4 v[70:73], v[26:33], v[58:65], 0
	s_setprio 0
	s_setprio 1
	v_mfma_f32_16x16x128_f8f6f4 v[130:133], v[2:9], v[34:41], 0
	v_mfma_f32_16x16x128_f8f6f4 v[126:129], v[10:17], v[34:41], 0
	v_mfma_f32_16x16x128_f8f6f4 v[114:117], v[2:9], v[42:49], 0
	v_mfma_f32_16x16x128_f8f6f4 v[110:113], v[10:17], v[42:49], 0
	s_add_i32 s98, s65, 0x2000
	s_mov_b32 m0, s98
	s_nop 0
	global_load_lds_dwordx4 v67, s[28:29]
	v_mfma_f32_16x16x128_f8f6f4 v[98:101], v[2:9], v[50:57], 0
	v_mfma_f32_16x16x128_f8f6f4 v[94:97], v[10:17], v[50:57], 0
	v_mfma_f32_16x16x128_f8f6f4 v[82:85], v[2:9], v[58:65], 0
	v_mfma_f32_16x16x128_f8f6f4 v[78:81], v[10:17], v[58:65], 0
	s_setprio 0
	s_barrier
; #define PG8_STAGE(bufoff, gbase, voff) do { PG8_GLDS((const char*)(gbase), (voff)[0], ldsb + (bufoff)); PG8_GLDS((const char*)(gbase), (voff)[1], ldsb + (bufoff) + 8192u); } while (0)
; #define PG8_STAGEA(bufoff, gbase, o0, o1) do { PG8_GLDS((const char*)(gbase), (o0), ldsb + (bufoff)); PG8_GLDS((const char*)(gbase), (o1), ldsb + (bufoff) + 8192u); } while (0)
; #define PG8_STAGEA1(bufoff, gbase) do { if constexpr (Sched::GATHER) { PG8_STAGEA(bufoff, gbase, vA2, vA3); } else { PG8_STAGEA(bufoff, (gbase) + hstep, vA0, vA1); } } while (0)
; #define PG8_LDA(dst, b, h) do { if constexpr (F8) { _Pragma("unroll") for (int m = 0; m < 4; ++m) dst##8[m] = PG8_LD32(lds + PG8_SA(b, h) + aoff + m * 2048); } else { \
;         _Pragma("unroll") for (int m = 0; m < 4; ++m) _Pragma("unroll") for (int k = 0; k < 2; ++k) dst[m][k] = *(const LAS bf16x8*)(lds + PG8_SA(b, h) + aoff + m * 2048 + k * 1024); } } while (0)
; #define PG8_LDB(dst, b, h) do { if constexpr (F8) { _Pragma("unroll") for (int n = 0; n < 2; ++n) dst##8[n] = PG8_LD32(lds + PG8_SB(b, h) + boff + n * 2048); } else { \
;         _Pragma("unroll") for (int n = 0; n < 2; ++n) _Pragma("unroll") for (int k = 0; k < 2; ++k) dst[n][k] = *(const LAS bf16x8*)(lds + PG8_SB(b, h) + boff + n * 2048 + k * 1024); } } while (0)
; #define PG8_WAIT_VR() PG8_WAIT_V(8)
; #define PG8_WAIT_L(n) asm volatile("s_waitcnt lgkmcnt(" #n ")" ::: "memory")
; #define PG8_BAR __builtin_amdgcn_s_barrier()
; #define PG8_SCHED __builtin_amdgcn_sched_barrier(0)
; template <class Epi, class Sched, bool F8 = false, bool PF = false, bool I8 = false, int PID = -1>
; __device__ __forceinline__ void gemm_phase(LAS unsigned char* lds, LAS unsigned char* xlds, const int RP, const int RPB, const int nt, const Sched& S, const Epi& E, const int stagger_ticks) {
;     ...
;             PG8_LDB(B0, 1, 0); PG8_LDB(B1, 1, 1); PG8_SCHED; PG8_LDA(At, 1, 0); PG8_STAGEA1(PG8_SA(0, 1), a2);
;             PG8_WAIT_VR(); PG8_WAIT_L(0); PG8_BAR; PG8_MMA(0, 0, At, B0); PG8_MMA(0, 1, At, B1); PG8_BAR; PG8_SCHED;
;             PG8_LDA(At, 1, 1); PG8_STAGE(PG8_SB(1, 0), b3, voffB); PG8_STAGE(PG8_SB(1, 1), b3 + hstepB, voffB); PG8_STAGEA(PG8_SA(1, 0), a3, vA0, vA1);
;             PG8_WAIT_VR(); PG8_WAIT_L(0); PG8_BAR; PG8_MMA(1, 0, At, B0); PG8_MMA(1, 1, At, B1); PG8_BAR; PG8_SCHED;
;         }
	v_add_u32_e32 v14, 0x18000, v206
	v_add_u32_e32 v30, 0x1c000, v206
	ds_read_b128 v[2:5], v14
	ds_read_b128 v[6:9], v14 offset:1024
	ds_read_b128 v[10:13], v14 offset:2048
	ds_read_b128 v[14:17], v14 offset:3072
	ds_read_b128 v[18:21], v30
	ds_read_b128 v[22:25], v30 offset:1024
	ds_read_b128 v[26:29], v30 offset:2048
	ds_read_b128 v[30:33], v30 offset:3072
	ds_read_b128 v[34:37], v207 offset:32768
	ds_read_b128 v[38:41], v207 offset:33792
	ds_read_b128 v[42:45], v207 offset:34816
	ds_read_b128 v[46:49], v207 offset:35840
	ds_read_b128 v[50:53], v207 offset:36864
	ds_read_b128 v[54:57], v207 offset:37888
	ds_read_b128 v[58:61], v207 offset:38912
	ds_read_b128 v[62:65], v207 offset:39936
	s_add_i32 s66, s65, 0x4000
	s_mov_b32 m0, s66
	s_nop 0
	global_load_lds_dwordx4 v68, s[28:29]
	s_add_i32 s66, s65, 0x6000
	s_mov_b32 m0, s66
	s_nop 0
	global_load_lds_dwordx4 v69, s[28:29]
	s_waitcnt vmcnt(8)
	s_waitcnt lgkmcnt(0)
	s_barrier
	s_setprio 1
	s_waitcnt lgkmcnt(6)
	v_mfma_f32_16x16x128_f8f6f4 v[186:189], v[2:9], v[34:41], v[186:189]
	v_mfma_f32_16x16x128_f8f6f4 v[194:197], v[10:17], v[34:41], v[194:197]
	s_waitcnt lgkmcnt(4)
	v_mfma_f32_16x16x128_f8f6f4 v[190:193], v[2:9], v[42:49], v[190:193]
	v_mfma_f32_16x16x128_f8f6f4 v[182:185], v[10:17], v[42:49], v[182:185]
	s_waitcnt lgkmcnt(2)
	v_mfma_f32_16x16x128_f8f6f4 v[154:157], v[2:9], v[50:57], v[154:157]
	v_mfma_f32_16x16x128_f8f6f4 v[150:153], v[10:17], v[50:57], v[150:153]
	s_waitcnt lgkmcnt(0)
	v_mfma_f32_16x16x128_f8f6f4 v[138:141], v[2:9], v[58:65], v[138:141]
	v_mfma_f32_16x16x128_f8f6f4 v[134:137], v[10:17], v[58:65], v[134:137]
	s_setprio 0
	s_setprio 1
	v_mfma_f32_16x16x128_f8f6f4 v[174:177], v[18:25], v[34:41], v[174:177]
	v_mfma_f32_16x16x128_f8f6f4 v[178:181], v[26:33], v[34:41], v[178:181]
	v_mfma_f32_16x16x128_f8f6f4 v[170:173], v[18:25], v[42:49], v[170:173]
	v_mfma_f32_16x16x128_f8f6f4 v[166:169], v[26:33], v[42:49], v[166:169]
	v_mfma_f32_16x16x128_f8f6f4 v[162:165], v[18:25], v[50:57], v[162:165]
	v_mfma_f32_16x16x128_f8f6f4 v[158:161], v[26:33], v[50:57], v[158:161]
	v_mfma_f32_16x16x128_f8f6f4 v[146:149], v[18:25], v[58:65], v[146:149]
	v_mfma_f32_16x16x128_f8f6f4 v[142:145], v[26:33], v[58:65], v[142:145]
	s_setprio 0
	s_barrier
	ds_read_b128 v[34:37], v207 offset:49152
	ds_read_b128 v[38:41], v207 offset:50176
	ds_read_b128 v[42:45], v207 offset:51200
	ds_read_b128 v[46:49], v207 offset:52224
	ds_read_b128 v[50:53], v207 offset:53248
	ds_read_b128 v[54:57], v207 offset:54272
	ds_read_b128 v[58:61], v207 offset:55296
	ds_read_b128 v[62:65], v207 offset:56320
	s_add_i32 s28, s65, 0x18000
	s_mov_b32 m0, s28
	s_nop 0
	global_load_lds_dwordx4 v204, s[30:31]
	s_add_i32 s28, s65, 0x1a000
	s_mov_b32 m0, s28
	s_nop 0
	global_load_lds_dwordx4 v205, s[30:31]
	s_add_u32 s26, s26, 0x2080
	s_addc_u32 s27, s27, 0
	s_add_i32 s28, s65, 0x1c000
	s_mov_b32 m0, s28
	s_nop 0
	global_load_lds_dwordx4 v204, s[26:27]
	s_add_i32 s28, s65, 0x1e000
	s_mov_b32 m0, s28
	s_nop 0
	global_load_lds_dwordx4 v205, s[26:27]
	s_waitcnt vmcnt(6)
	s_waitcnt lgkmcnt(0)
	s_barrier
	s_setprio 1
	s_waitcnt lgkmcnt(6)
	v_mfma_f32_16x16x128_f8f6f4 v[122:125], v[2:9], v[34:41], v[122:125]
	v_mfma_f32_16x16x128_f8f6f4 v[118:121], v[10:17], v[34:41], v[118:121]
	s_waitcnt lgkmcnt(4)
	v_mfma_f32_16x16x128_f8f6f4 v[106:109], v[2:9], v[42:49], v[106:109]
	v_mfma_f32_16x16x128_f8f6f4 v[102:105], v[10:17], v[42:49], v[102:105]
	s_add_i32 s98, s65, 0x8000
	s_mov_b32 m0, s98
	s_nop 0
	global_load_lds_dwordx4 v66, s[24:25]
	s_waitcnt lgkmcnt(2)
	v_mfma_f32_16x16x128_f8f6f4 v[90:93], v[2:9], v[50:57], v[90:93]
	v_mfma_f32_16x16x128_f8f6f4 v[86:89], v[10:17], v[50:57], v[86:89]
	s_waitcnt lgkmcnt(0)
	v_mfma_f32_16x16x128_f8f6f4 v[74:77], v[2:9], v[58:65], v[74:77]
	v_mfma_f32_16x16x128_f8f6f4 v[70:73], v[10:17], v[58:65], v[70:73]
	s_setprio 0
	s_setprio 1
	v_mfma_f32_16x16x128_f8f6f4 v[130:133], v[18:25], v[34:41], v[130:133]
	v_mfma_f32_16x16x128_f8f6f4 v[126:129], v[26:33], v[34:41], v[126:129]
	v_mfma_f32_16x16x128_f8f6f4 v[114:117], v[18:25], v[42:49], v[114:117]
	v_mfma_f32_16x16x128_f8f6f4 v[110:113], v[26:33], v[42:49], v[110:113]
	s_add_i32 s98, s65, 0xa000
	s_mov_b32 m0, s98
	s_nop 0
	global_load_lds_dwordx4 v67, s[24:25]
	v_mfma_f32_16x16x128_f8f6f4 v[98:101], v[18:25], v[50:57], v[98:101]
	v_mfma_f32_16x16x128_f8f6f4 v[94:97], v[26:33], v[50:57], v[94:97]
	v_mfma_f32_16x16x128_f8f6f4 v[82:85], v[18:25], v[58:65], v[82:85]
	v_mfma_f32_16x16x128_f8f6f4 v[78:81], v[26:33], v[58:65], v[78:81]
	s_setprio 0
	s_barrier
	s_add_i32 s64, s64, 2
	s_add_u32 s23, s23, 0x100
	s_addc_u32 s63, s63, 0
	s_add_u32 s2, s2, 0x100
	s_addc_u32 s3, s3, 0
	s_cmp_gt_u32 s64, 5
	s_branch .LBB0_959

; #define PG8_BAR __builtin_amdgcn_s_barrier()
; template <class Epi, class Sched, bool F8 = false, bool PF = false, bool I8 = false, int PID = -1>
; __device__ __forceinline__ void gemm_phase(LAS unsigned char* lds, LAS unsigned char* xlds, const int RP, const int RPB, const int nt, const Sched& S, const Epi& E, const int stagger_ticks) {
;     ...
;         if (Sched::GATHER) { *nslot = (u32x4){gv[0], gv[1], gv[2], gv[3]}; asm volatile("" ::: "memory"); }
;         PG8_ZERO_ACC();
;         if (wr == 1) PG8_BAR;
.Lmy_gvdone:
	v_mov_b32_e32 v199, v198
	ds_write_b128 v203, v[2:5]
	v_mov_b64_e32 v[2:3], v[198:199]
	s_andn2_b64 vcc, exec, s[12:13]
	s_cbranch_vccnz .LBB0_955
	s_barrier
	s_branch .LBB0_955
